# baseline (speedup 1.0000x reference)
.LBB1_4:
	s_movk_i32 s5, 0x1010
	v_mad_u32_u24 v0, v73, s5, v56
	s_waitcnt lgkmcnt(0)
	s_barrier
	ds_read_b128 v[18:21], v0
	s_waitcnt vmcnt(3)
	v_pk_add_f32 v[22:23], s[4:5], v[16:17] op_sel_hi:[0,1]
	v_pk_add_f32 v[24:25], s[4:5], v[14:15] op_sel_hi:[0,1]
	ds_read_b128 v[14:17], v0 offset:1024
	s_waitcnt vmcnt(2)
	v_pk_add_f32 v[12:13], s[4:5], v[12:13] op_sel_hi:[0,1]
	s_waitcnt lgkmcnt(1)
	v_pk_add_f32 v[22:23], v[20:21], v[22:23]
	v_pk_add_f32 v[24:25], v[18:19], v[24:25]
	v_pk_add_f32 v[10:11], s[4:5], v[10:11] op_sel_hi:[0,1]
	v_cndmask_b32_e64 v21, v21, v23, s[2:3]
	v_cndmask_b32_e64 v20, v20, v22, s[2:3]
	v_cndmask_b32_e64 v22, v19, v25, s[2:3]
	v_cndmask_b32_e64 v23, v18, v24, s[2:3]
	s_waitcnt lgkmcnt(0)
	v_pk_add_f32 v[12:13], v[16:17], v[12:13]
	v_pk_add_f32 v[18:19], v[14:15], v[10:11]
	v_cndmask_b32_e64 v24, v17, v13, s[2:3]
	v_cndmask_b32_e64 v25, v16, v12, s[2:3]
	v_cndmask_b32_e64 v19, v15, v19, s[2:3]
	ds_read_b128 v[10:13], v0 offset:2048
	v_cndmask_b32_e64 v18, v14, v18, s[2:3]
	s_waitcnt vmcnt(1)
	v_pk_add_f32 v[14:15], s[4:5], v[8:9] op_sel_hi:[0,1]
	v_pk_add_f32 v[16:17], s[4:5], v[6:7] op_sel_hi:[0,1]
	ds_read_b128 v[6:9], v0 offset:3072
	s_waitcnt vmcnt(0)
	v_pk_add_f32 v[4:5], s[4:5], v[4:5] op_sel_hi:[0,1]
	v_cmp_ne_u16_e32 vcc, 0, v72
	s_cmp_lg_u64 vcc, 0
	v_and_b32_e32 v26, 0xffff, v72
	s_waitcnt lgkmcnt(0)
	v_pk_add_f32 v[4:5], v[8:9], v[4:5]
	s_cselect_b64 vcc, -1, 0
	v_cndmask_b32_e64 v4, v8, v4, s[2:3]
	v_mov_b32_e32 v8, 0xffff
	v_pk_add_f32 v[14:15], v[12:13], v[14:15]
	v_cndmask_b32_e32 v8, v8, v26, vcc
	v_cndmask_b32_e64 v0, v13, v15, s[2:3]
	v_and_b32_e32 v13, 1, v8
	v_pk_add_f32 v[16:17], v[10:11], v[16:17]
	v_cndmask_b32_e64 v12, v12, v14, s[2:3]
	v_cndmask_b32_e64 v5, v9, v5, s[2:3]
	v_mul_f32_e32 v9, 0x3fb8aa3b, v23
	v_mov_b32_e32 v14, 0xff800000
	v_cmp_eq_u32_e32 vcc, 1, v13
	v_and_b32_e32 v15, 2, v8
	v_cndmask_b32_e64 v11, v11, v17, s[2:3]
	v_cndmask_b32_e32 v9, v14, v9, vcc
	v_mul_f32_e32 v13, 0x3fb8aa3b, v22
	v_cmp_ne_u32_e32 vcc, 0, v15
	v_and_b32_e32 v17, 4, v8
	v_cndmask_b32_e64 v10, v10, v16, s[2:3]
	v_cndmask_b32_e32 v13, v14, v13, vcc
	v_mul_f32_e32 v16, 0x3fb8aa3b, v20
	v_cmp_ne_u32_e32 vcc, 0, v17
	v_and_b32_e32 v20, 8, v8
	v_mul_f32_e32 v17, 0x3fb8aa3b, v21
	v_cndmask_b32_e32 v16, v14, v16, vcc
	v_cmp_ne_u32_e32 vcc, 0, v20
	v_and_b32_e32 v20, 16, v8
	v_pk_add_f32 v[2:3], s[4:5], v[2:3] op_sel_hi:[0,1]
	v_cndmask_b32_e32 v17, v14, v17, vcc
	v_mul_f32_e32 v18, 0x3fb8aa3b, v18
	v_cmp_ne_u32_e32 vcc, 0, v20
	v_and_b32_e32 v20, 32, v8
	v_pk_add_f32 v[2:3], v[6:7], v[2:3]
	v_cndmask_b32_e32 v18, v14, v18, vcc
	v_mul_f32_e32 v19, 0x3fb8aa3b, v19
	v_cmp_ne_u32_e32 vcc, 0, v20
	v_and_b32_e32 v21, 64, v8
	v_cndmask_b32_e64 v7, v7, v3, s[2:3]
	v_cndmask_b32_e64 v6, v6, v2, s[2:3]
	v_lshlrev_b64 v[2:3], 12, v[54:55]
	v_cndmask_b32_e32 v19, v14, v19, vcc
	v_mul_f32_e32 v20, 0x3fb8aa3b, v25
	v_cmp_ne_u32_e32 vcc, 0, v21
	v_and_b32_e32 v22, 0x80, v8
	v_lshl_add_u64 v[2:3], s[0:1], 0, v[2:3]
	s_mov_b32 s0, 0xff800000
	v_cndmask_b32_e32 v20, v14, v20, vcc
	v_mul_f32_e32 v21, 0x3fb8aa3b, v24
	v_cmp_ne_u32_e32 vcc, 0, v22
	v_and_b32_e32 v22, 0x100, v8
	v_max3_f32 v15, v9, s0, v13
	v_cndmask_b32_e32 v21, v14, v21, vcc
	v_mul_f32_e32 v10, 0x3fb8aa3b, v10
	v_cmp_ne_u32_e32 vcc, 0, v22
	v_max3_f32 v15, v15, v16, v17
	v_max3_f32 v15, v15, v18, v19
	v_cndmask_b32_e32 v22, v14, v10, vcc
	v_mul_f32_e32 v10, 0x3fb8aa3b, v11
	v_and_b32_e32 v11, 0x200, v8
	v_cmp_ne_u32_e32 vcc, 0, v11
	v_mul_f32_e32 v11, 0x3fb8aa3b, v12
	v_and_b32_e32 v12, 0x400, v8
	v_max3_f32 v15, v15, v20, v21
	v_cndmask_b32_e32 v23, v14, v10, vcc
	v_cmp_ne_u32_e32 vcc, 0, v12
	v_max3_f32 v10, v15, v22, v23
	v_mul_f32_e32 v0, 0x3fb8aa3b, v0
	v_cndmask_b32_e32 v15, v14, v11, vcc
	v_and_b32_e32 v11, 0x800, v8
	v_cmp_ne_u32_e32 vcc, 0, v11
	v_and_b32_e32 v11, 0x1000, v8
	v_mul_f32_e32 v6, 0x3fb8aa3b, v6
	v_cndmask_b32_e32 v0, v14, v0, vcc
	v_cmp_ne_u32_e32 vcc, 0, v11
	v_mul_f32_e32 v4, 0x3fb8aa3b, v4
	s_movk_i32 s0, 0x7fff
	v_cndmask_b32_e32 v24, v14, v6, vcc
	v_mul_f32_e32 v6, 0x3fb8aa3b, v7
	v_and_b32_e32 v7, 0x2000, v8
	v_cmp_ne_u32_e32 vcc, 0, v7
	v_and_b32_e32 v7, 0x4000, v8
	v_max3_f32 v10, v10, v15, v0
	v_cndmask_b32_e32 v25, v14, v6, vcc
	v_cmp_ne_u32_e32 vcc, 0, v7
	v_max3_f32 v6, v10, v24, v25
	s_nop 0
	v_cndmask_b32_e32 v26, v14, v4, vcc
	v_mul_f32_e32 v4, 0x3fb8aa3b, v5
	v_cmp_lt_u32_e32 vcc, s0, v8
	v_mov_b32_e32 v5, 0
	s_nop 0
	v_cndmask_b32_e32 v27, v14, v4, vcc
	v_max3_f32 v4, v6, v26, v27
	s_nop 1
	v_mov_b32_dpp v5, v4 quad_perm:[1,0,3,2] row_mask:0xf bank_mask:0xf
	v_max_f32_e32 v5, v5, v5
	v_max_f32_e32 v4, v4, v5
	v_mov_b32_e32 v5, 0
	s_nop 1
	v_mov_b32_dpp v5, v4 quad_perm:[2,3,0,1] row_mask:0xf bank_mask:0xf
	v_max_f32_e32 v5, v5, v5
	v_max_f32_e32 v4, v4, v5
	v_mov_b32_e32 v5, 0
	s_nop 1
	v_mov_b32_dpp v5, v4 row_half_mirror row_mask:0xf bank_mask:0xf
	v_max_f32_e32 v5, v5, v5
	v_max_f32_e32 v4, v4, v5
	v_mov_b32_e32 v5, 0
	s_nop 1
	v_mov_b32_dpp v5, v4 row_mirror row_mask:0xf bank_mask:0xf
	v_max_f32_e32 v5, v5, v5
	v_max_f32_e32 v4, v4, v5
	s_nop 0
	v_readlane_b32 s2, v4, 32
	v_readlane_b32 s3, v4, 48
	v_readlane_b32 s0, v4, 0
	v_readlane_b32 s1, v4, 16
	v_max_f32_e64 v4, s3, s3
	v_max_f32_e64 v5, s2, s2
	v_max_f32_e32 v4, v5, v4
	v_mov_b32_e32 v5, s1
	v_max3_f32 v28, s0, v5, v4
	v_sub_f32_e32 v4, v9, v28
	v_exp_f32_e32 v4, v4
	v_sub_f32_e32 v5, v13, v28
	v_exp_f32_e32 v5, v5
	v_sub_f32_e32 v6, v16, v28
	v_exp_f32_e32 v6, v6
	v_sub_f32_e32 v7, v17, v28
	v_exp_f32_e32 v7, v7
	v_add_f32_e32 v8, 0, v4
	v_add_f32_e32 v8, v8, v5
	v_add_f32_e32 v8, v8, v6
	v_add_f32_e32 v12, v8, v7
	v_sub_f32_e32 v8, v18, v28
	v_exp_f32_e32 v8, v8
	v_sub_f32_e32 v9, v19, v28
	v_exp_f32_e32 v9, v9
	v_sub_f32_e32 v10, v20, v28
	v_exp_f32_e32 v10, v10
	v_sub_f32_e32 v11, v21, v28
	v_exp_f32_e32 v11, v11
	v_add_f32_e32 v12, v12, v8
	v_add_f32_e32 v12, v12, v9
	v_add_f32_e32 v12, v12, v10
	v_add_f32_e32 v16, v12, v11
	v_sub_f32_e32 v12, v22, v28
	v_exp_f32_e32 v12, v12
	v_sub_f32_e32 v13, v23, v28
	v_exp_f32_e32 v13, v13
	v_sub_f32_e32 v14, v15, v28
	v_exp_f32_e32 v14, v14
	v_sub_f32_e32 v0, v0, v28
	v_exp_f32_e32 v15, v0
	v_add_f32_e32 v0, v16, v12
	v_sub_f32_e32 v16, v24, v28
	v_exp_f32_e32 v16, v16
	v_sub_f32_e32 v17, v25, v28
	v_add_f32_e32 v0, v0, v13
	v_exp_f32_e32 v17, v17
	v_sub_f32_e32 v18, v26, v28
	v_add_f32_e32 v0, v0, v14
	v_exp_f32_e32 v18, v18
	v_sub_f32_e32 v19, v27, v28
	v_add_f32_e32 v0, v0, v15
	v_exp_f32_e32 v19, v19
	v_add_f32_e32 v0, v0, v16
	v_add_f32_e32 v0, v0, v17
	v_add_f32_e32 v0, v0, v18
	v_add_f32_e32 v0, v0, v19
	s_nop 1
	v_add_f32_dpp v0, v0, v0 quad_perm:[1,0,3,2] row_mask:0xf bank_mask:0xf bound_ctrl:1
	s_nop 1
	v_add_f32_dpp v0, v0, v0 quad_perm:[2,3,0,1] row_mask:0xf bank_mask:0xf bound_ctrl:1
	s_nop 1
	v_add_f32_dpp v0, v0, v0 row_half_mirror row_mask:0xf bank_mask:0xf bound_ctrl:1
	s_nop 1
	v_add_f32_dpp v0, v0, v0 row_mirror row_mask:0xf bank_mask:0xf bound_ctrl:1
	s_nop 0
	v_readlane_b32 s2, v0, 16
	v_readlane_b32 s3, v0, 48
	v_readlane_b32 s0, v0, 0
	v_readlane_b32 s1, v0, 32
	v_mov_b32_e32 v20, s2
	v_mov_b32_e32 v21, s3
	v_pk_add_f32 v[20:21], s[0:1], v[20:21]
	s_nop 0
	v_add_f32_e32 v0, v20, v21
	v_div_scale_f32 v22, s[0:1], v0, v0, 1.0
	v_rcp_f32_e32 v23, v22
	v_lshlrev_b32_e32 v20, 2, v1
	v_mov_b32_e32 v21, 0
	v_lshl_add_u64 v[20:21], v[2:3], 0, v[20:21]
	v_fma_f32 v1, -v22, v23, 1.0
	v_fmac_f32_e32 v23, v1, v23
	v_div_scale_f32 v1, vcc, 1.0, v0, 1.0
	v_mul_f32_e32 v2, v1, v23
	v_fma_f32 v3, -v22, v2, v1
	v_fmac_f32_e32 v2, v3, v23
	v_fma_f32 v1, -v22, v2, v1
	v_div_fmas_f32 v1, v1, v23, v2
	v_div_fixup_f32 v22, v1, v0, 1.0
	v_pk_mul_f32 v[2:3], v[22:23], v[6:7] op_sel_hi:[0,1]
	v_pk_mul_f32 v[0:1], v[22:23], v[4:5] op_sel_hi:[0,1]
	global_store_dwordx4 v[20:21], v[0:3], off sc1 nt
	s_nop 1
	v_pk_mul_f32 v[2:3], v[22:23], v[10:11] op_sel_hi:[0,1]
	v_pk_mul_f32 v[0:1], v[22:23], v[8:9] op_sel_hi:[0,1]
	global_store_dwordx4 v[20:21], v[0:3], off offset:1024 sc1 nt
	s_nop 1
	v_pk_mul_f32 v[2:3], v[22:23], v[14:15] op_sel_hi:[0,1]
	v_pk_mul_f32 v[0:1], v[22:23], v[12:13] op_sel_hi:[0,1]
	global_store_dwordx4 v[20:21], v[0:3], off offset:2048 sc1 nt
	s_nop 1
	v_pk_mul_f32 v[2:3], v[22:23], v[18:19] op_sel_hi:[0,1]
	v_pk_mul_f32 v[0:1], v[22:23], v[16:17] op_sel_hi:[0,1]
	global_store_dwordx4 v[20:21], v[0:3], off offset:3072 sc1 nt
	s_endpgm
